# speedup vs baseline: 1.0169x; 1.0169x over previous
_Z9ssim_mainPKfS0_S0_Pf:
	v_readfirstlane_b32 s29, v0
	s_load_dwordx4 s[4:7], s[0:1], 0x0
	s_load_dwordx4 s[8:11], s[0:1], 0x10
	s_mov_b32 s51, 0x44800000
	s_mov_b32 s38, 0
	s_mov_b32 s39, -1
	s_lshr_b32 s12, s29, 6
	s_and_b32 s52, s12, 3
	s_lshl_b32 s52, s52, 1
	s_lshr_b32 s53, s12, 2
	s_or_b32 s52, s52, s53
	s_mov_b32 s13, s2
	s_lshr_b32 s14, s13, 3
	s_and_b32 s15, s13, 7
	s_lshl_b32 s16, s14, 20
	s_lshl_b32 s17, s15, 17
	s_add_u32 s16, s16, s17
	s_lshl_b32 s17, s52, 8
	s_add_u32 s16, s16, s17
	s_lshl_b32 s27, s52, 2
	s_add_u32 s27, s27, 0x10000
	v_and_b32_e32 v8, 63, v0
	v_and_b32_e32 v169, 15, v0
	v_bfe_u32 v164, v0, 4, 2
	v_lshrrev_b32_e32 v167, 2, v169
	v_lshlrev_b32_e32 v167, 5, v167
	v_and_b32_e32 v168, 1, v169
	v_lshl_or_b32 v167, v168, 4, v167
	v_bfe_u32 v168, v169, 1, 1
	v_lshl_or_b32 v167, v168, 7, v167
	v_lshl_or_b32 v9, v164, 14, v167
	v_and_b32_e32 v168, 1, v164
	v_lshl_or_b32 v23, v168, 14, v167
	v_lshrrev_b32_e32 v168, 1, v164
	v_lshl_or_b32 v23, v168, 13, v23
	v_add_u32_e32 v237, 0x1000, v9
	v_add_u32_e32 v238, 0x2000, v9
	v_add_u32_e32 v239, 0x3000, v9
	v_add_u32_e32 v240, 0x10000, v9
	v_add_u32_e32 v241, 0x11000, v9
	v_add_u32_e32 v242, 0x12000, v9
	v_add_u32_e32 v243, 0x13000, v9
	s_waitcnt lgkmcnt(0)
	s_load_dwordx8 s[40:47], s[8:9], 0x0
	s_load_dwordx2 s[48:49], s[8:9], 0x20
	s_load_dword s50, s[8:9], 0x28
	s_add_u32 s18, s4, s16
	s_addc_u32 s19, s5, 0
	s_add_u32 s20, s6, s16
	s_addc_u32 s21, s7, 0
	global_load_dwordx4 v[36:39], v9, s[18:19] offset:0 sc1 nt
	global_load_dwordx4 v[40:43], v9, s[18:19] offset:2048 sc1 nt
	global_load_dwordx4 v[68:71], v9, s[20:21] offset:0 sc1 nt
	global_load_dwordx4 v[72:75], v9, s[20:21] offset:2048 sc1 nt
	global_load_dwordx4 v[44:47], v237, s[18:19] offset:0 sc1 nt
	global_load_dwordx4 v[48:51], v237, s[18:19] offset:2048 sc1 nt
	global_load_dwordx4 v[76:79], v237, s[20:21] offset:0 sc1 nt
	global_load_dwordx4 v[80:83], v237, s[20:21] offset:2048 sc1 nt
	global_load_dwordx4 v[52:55], v238, s[18:19] offset:0 sc1 nt
	global_load_dwordx4 v[56:59], v238, s[18:19] offset:2048 sc1 nt
	global_load_dwordx4 v[84:87], v238, s[20:21] offset:0 sc1 nt
	global_load_dwordx4 v[88:91], v238, s[20:21] offset:2048 sc1 nt
	global_load_dwordx4 v[60:63], v239, s[18:19] offset:0 sc1 nt
	global_load_dwordx4 v[64:67], v239, s[18:19] offset:2048 sc1 nt
	global_load_dwordx4 v[92:95], v239, s[20:21] offset:0 sc1 nt
	global_load_dwordx4 v[96:99], v239, s[20:21] offset:2048 sc1 nt
	v_mov_b32_e32 v6, s27
	v_mov_b32_e32 v168, 0
	ds_write_b32 v6, v168 offset:0
	ds_write_b32 v6, v168 offset:32
	ds_write_b32 v6, v168 offset:64
	ds_write_b32 v6, v168 offset:96
	v_lshlrev_b32_e32 v167, 3, v164
	v_xor_b32_e32 v168, 16, v167
	v_sub_u32_e32 v165, v167, v169
	v_sub_u32_e32 v166, v168, v169
	v_add_u32_e32 v172, 0, v165
	v_min_u32_e32 v172, 11, v172
	v_lshlrev_b32_e32 v172, 2, v172
	v_add_u32_e32 v173, 1, v165
	v_min_u32_e32 v173, 11, v173
	v_lshlrev_b32_e32 v173, 2, v173
	v_add_u32_e32 v174, 2, v165
	v_min_u32_e32 v174, 11, v174
	v_lshlrev_b32_e32 v174, 2, v174
	v_add_u32_e32 v175, 3, v165
	v_min_u32_e32 v175, 11, v175
	v_lshlrev_b32_e32 v175, 2, v175
	v_add_u32_e32 v176, 4, v165
	v_min_u32_e32 v176, 11, v176
	v_lshlrev_b32_e32 v176, 2, v176
	v_add_u32_e32 v177, 5, v165
	v_min_u32_e32 v177, 11, v177
	v_lshlrev_b32_e32 v177, 2, v177
	v_add_u32_e32 v178, 6, v165
	v_min_u32_e32 v178, 11, v178
	v_lshlrev_b32_e32 v178, 2, v178
	v_add_u32_e32 v179, 7, v165
	v_min_u32_e32 v179, 11, v179
	v_lshlrev_b32_e32 v179, 2, v179
	v_add_u32_e32 v180, 0, v166
	v_min_u32_e32 v180, 11, v180
	v_lshlrev_b32_e32 v180, 2, v180
	v_add_u32_e32 v181, 1, v166
	v_min_u32_e32 v181, 11, v181
	v_lshlrev_b32_e32 v181, 2, v181
	v_add_u32_e32 v182, 2, v166
	v_min_u32_e32 v182, 11, v182
	v_lshlrev_b32_e32 v182, 2, v182
	v_add_u32_e32 v183, 3, v166
	v_min_u32_e32 v183, 11, v183
	v_lshlrev_b32_e32 v183, 2, v183
	v_add_u32_e32 v184, 4, v166
	v_min_u32_e32 v184, 11, v184
	v_lshlrev_b32_e32 v184, 2, v184
	v_add_u32_e32 v185, 5, v166
	v_min_u32_e32 v185, 11, v185
	v_lshlrev_b32_e32 v185, 2, v185
	v_add_u32_e32 v186, 6, v166
	v_min_u32_e32 v186, 11, v186
	v_lshlrev_b32_e32 v186, 2, v186
	v_add_u32_e32 v187, 7, v166
	v_min_u32_e32 v187, 11, v187
	v_lshlrev_b32_e32 v187, 2, v187
	s_cmp_eq_u32 s15, 7
	s_cselect_b32 s22, 0, 0x20000
	s_add_u32 s84, s18, s22
	s_addc_u32 s85, s19, 0
	s_add_u32 s86, s18, s22
	s_addc_u32 s87, s19, 0
	s_add_u32 s86, s86, 0x1000
	s_addc_u32 s87, s87, 0
	s_add_u32 s88, s20, s22
	s_addc_u32 s89, s21, 0
	s_add_u32 s90, s20, s22
	s_addc_u32 s91, s21, 0
	s_add_u32 s90, s90, 0x1000
	s_addc_u32 s91, s91, 0
	s_waitcnt lgkmcnt(0)
	v_writelane_b32 v171, s40, 0
	v_writelane_b32 v171, s41, 1
	v_writelane_b32 v171, s42, 2
	v_writelane_b32 v171, s43, 3
	v_writelane_b32 v171, s44, 4
	v_writelane_b32 v171, s45, 5
	v_writelane_b32 v171, s46, 6
	v_writelane_b32 v171, s47, 7
	v_writelane_b32 v171, s48, 8
	v_writelane_b32 v171, s49, 9
	v_writelane_b32 v171, s50, 10
	v_writelane_b32 v171, 0, 11
	v_fma_mixlo_f16 v171, v171, s51, 0
	ds_bpermute_b32 v188, v172, v171
	ds_bpermute_b32 v189, v173, v171
	ds_bpermute_b32 v190, v174, v171
	ds_bpermute_b32 v191, v175, v171
	ds_bpermute_b32 v192, v176, v171
	ds_bpermute_b32 v193, v177, v171
	ds_bpermute_b32 v194, v178, v171
	ds_bpermute_b32 v195, v179, v171
	v_mov_b32_e32 v229, 0x44800000
	v_fma_mixlo_f16 v228, s40, v229, 0
	v_cvt_f32_f16_e32 v228, v228
	v_cvt_f64_f32_e32 v[212:213], v228
	v_add_f64 v[212:213], v[212:213], 0
	v_fma_mixlo_f16 v228, s41, v229, 0
	v_cvt_f32_f16_e32 v228, v228
	v_cvt_f64_f32_e32 v[214:215], v228
	v_add_f64 v[212:213], v[212:213], v[214:215]
	v_fma_mixlo_f16 v228, s42, v229, 0
	v_cvt_f32_f16_e32 v228, v228
	v_cvt_f64_f32_e32 v[214:215], v228
	v_add_f64 v[212:213], v[212:213], v[214:215]
	v_fma_mixlo_f16 v228, s43, v229, 0
	v_cvt_f32_f16_e32 v228, v228
	v_cvt_f64_f32_e32 v[214:215], v228
	v_add_f64 v[212:213], v[212:213], v[214:215]
	v_fma_mixlo_f16 v228, s44, v229, 0
	v_cvt_f32_f16_e32 v228, v228
	v_cvt_f64_f32_e32 v[214:215], v228
	v_add_f64 v[212:213], v[212:213], v[214:215]
	v_fma_mixlo_f16 v228, s45, v229, 0
	v_cvt_f32_f16_e32 v228, v228
	v_cvt_f64_f32_e32 v[214:215], v228
	v_add_f64 v[212:213], v[212:213], v[214:215]
	v_fma_mixlo_f16 v228, s46, v229, 0
	v_cvt_f32_f16_e32 v228, v228
	v_cvt_f64_f32_e32 v[214:215], v228
	v_add_f64 v[212:213], v[212:213], v[214:215]
	v_fma_mixlo_f16 v228, s47, v229, 0
	v_cvt_f32_f16_e32 v228, v228
	v_cvt_f64_f32_e32 v[214:215], v228
	v_add_f64 v[212:213], v[212:213], v[214:215]
	v_fma_mixlo_f16 v228, s48, v229, 0
	v_cvt_f32_f16_e32 v228, v228
	v_cvt_f64_f32_e32 v[214:215], v228
	v_add_f64 v[212:213], v[212:213], v[214:215]
	v_fma_mixlo_f16 v228, s49, v229, 0
	v_cvt_f32_f16_e32 v228, v228
	v_cvt_f64_f32_e32 v[214:215], v228
	v_add_f64 v[212:213], v[212:213], v[214:215]
	v_fma_mixlo_f16 v228, s50, v229, 0
	v_cvt_f32_f16_e32 v228, v228
	v_cvt_f64_f32_e32 v[214:215], v228
	v_add_f64 v[212:213], v[212:213], v[214:215]
	s_waitcnt lgkmcnt(7)
	ds_bpermute_b32 v196, v180, v171
	ds_bpermute_b32 v197, v181, v171
	ds_bpermute_b32 v198, v182, v171
	ds_bpermute_b32 v199, v183, v171
	ds_bpermute_b32 v200, v184, v171
	ds_bpermute_b32 v201, v185, v171
	ds_bpermute_b32 v202, v186, v171
	ds_bpermute_b32 v203, v187, v171
	v_mul_f64 v[212:213], v[212:213], v[212:213]
	v_mul_f64 v[216:217], v[212:213], 0.5
	v_add_f64 v[218:219], v[216:217], v[216:217]
	s_mov_b32 s36, 0xeb1c432d
	s_mov_b32 s37, 0x3f1a36e2
	v_mul_f64 v[220:221], v[212:213], s[36:37]
	v_mul_f64 v[222:223], v[216:217], v[218:219]
	v_fmac_f64_e32 v[222:223], v[212:213], v[220:221]
	v_add_f64 v[224:225], v[212:213], v[212:213]
	s_mov_b32 s36, 0x487fcb92
	s_mov_b32 s37, 0x3f4d7dbf
	v_mul_f64 v[226:227], v[212:213], s[36:37]
	v_cvt_f32_f64_e32 v0, v[226:227]
	v_mov_b32_e32 v1, v0
	v_mov_b32_e32 v2, v0
	v_mov_b32_e32 v3, v0
	v_cvt_f32_f64_e32 v10, v[218:219]
	v_cvt_f32_f64_e32 v11, v[222:223]
	v_cvt_f32_f64_e32 v12, v[212:213]
	v_cvt_f32_f64_e32 v13, v[224:225]
	v_mul_f64 v[226:227], v[212:213], v[226:227]
	v_cvt_f32_f64_e32 v14, v[226:227]
	v_lshlrev_b32_e32 v167, 2, v164
	s_cmp_eq_u32 s52, 0
	s_cselect_b32 s23, 6, 64
	v_add_u32_e32 v168, 0, v167
	v_cmp_gt_u32_e32 vcc, s23, v168
	s_nop 1
	v_cndmask_b32_e64 v15, 0, 1.0, vcc
	v_add_u32_e32 v168, 1, v167
	v_cmp_gt_u32_e32 vcc, s23, v168
	s_nop 1
	v_cndmask_b32_e64 v16, 0, 1.0, vcc
	v_add_u32_e32 v168, 2, v167
	v_cmp_gt_u32_e32 vcc, s23, v168
	s_nop 1
	v_cndmask_b32_e64 v17, 0, 1.0, vcc
	v_add_u32_e32 v168, 3, v167
	v_cmp_gt_u32_e32 vcc, s23, v168
	s_nop 1
	v_cndmask_b32_e64 v18, 0, 1.0, vcc
	v_and_b32_e32 v167, 31, v8
	v_lshlrev_b32_e32 v167, 4, v167
	s_lshl_b32 s24, s52, 11
	s_add_i32 s25, s52, 7
	s_and_b32 s25, s25, 7
	s_lshl_b32 s26, s25, 11
	v_or_b32_e32 v4, s24, v167
	v_or_b32_e32 v5, s26, v167
	s_lshl_b32 s28, s25, 2
	s_add_u32 s28, s28, 0x10000
	v_mov_b32_e32 v7, s28
	v_mov_b32_e32 v19, 0
	v_mov_b32_e32 v20, 0
	v_mov_b32_e32 v21, 0
	v_mov_b32_e32 v22, 0
	s_waitcnt lgkmcnt(0)
	v_cmp_lt_u32_e64 s[32:33], 31, v8
	v_cmp_gt_u32_e64 s[34:35], 32, v8
	v_pack_b32_f16 v24, v188, v189
	v_pack_b32_f16 v25, v190, v191
	v_pack_b32_f16 v26, v192, v193
	v_pack_b32_f16 v27, v194, v195
	v_pack_b32_f16 v167, v196, v197
	v_cndmask_b32_e64 v28, 0, v167, s[32:33]
	v_cndmask_b32_e64 v32, 0, v167, s[34:35]
	v_pack_b32_f16 v167, v198, v199
	v_cndmask_b32_e64 v29, 0, v167, s[32:33]
	v_cndmask_b32_e64 v33, 0, v167, s[34:35]
	v_pack_b32_f16 v167, v200, v201
	v_cndmask_b32_e64 v30, 0, v167, s[32:33]
	v_cndmask_b32_e64 v34, 0, v167, s[34:35]
	v_pack_b32_f16 v167, v202, v203
	v_cndmask_b32_e64 v31, 0, v167, s[32:33]
	v_cndmask_b32_e64 v35, 0, v167, s[34:35]
	s_waitcnt lgkmcnt(0)
	s_barrier
	s_cmp_lt_u32 s12, 4
	s_cbranch_scc1 .Lq_noprio
	s_setprio 1

.Lq_go_3:
	ds_read_b128 v[228:231], v5 offset:49152
	ds_read_b128 v[232:235], v5 offset:49664
	ds_read_b128 v[236:239], v5 offset:50176
	ds_read_b128 v[240:243], v5 offset:50688
	v_mul_f32_e32 v244, v212, v216
	v_mul_f32_e32 v250, v213, v217
	v_mul_f32_e64 v245, -v216, v216
	v_mul_f32_e64 v251, -v217, v217
	v_add_f32_e32 v246, v212, v216
	v_add_f32_e32 v252, v213, v217
	v_fma_f32 v245, -v212, v212, v245
	v_fma_f32 v251, -v213, v213, v251
	v_fma_f32 v247, v10, v246, v11
	v_fma_f32 v253, v10, v252, v11
	v_fma_f32 v246, v13, v224, v14
	v_fma_f32 v252, v13, v225, v14
	v_fma_f32 v248, v12, v220, v245
	v_fma_f32 v254, v12, v221, v251
	v_fma_f32 v249, 2.0, v244, v247
	v_fma_f32 v255, 2.0, v250, v253
	v_sub_f32_e32 v247, v247, v245
	v_sub_f32_e32 v253, v253, v251
	v_fma_f32 v246, -2.0, v244, v246
	v_fma_f32 v252, -2.0, v250, v252
	v_mul_f32_e32 v247, v247, v248
	v_mul_f32_e32 v253, v253, v254
	v_rcp_f32_e32 v247, v247
	v_rcp_f32_e32 v253, v253
	v_mul_f32_e32 v249, v249, v246
	v_mul_f32_e32 v255, v255, v252
	v_fma_f32 v21, v249, v247, v21
	v_fma_f32 v21, v255, v253, v21
	v_mul_f32_e32 v244, v214, v218
	v_mul_f32_e32 v250, v215, v219
	v_mul_f32_e64 v245, -v218, v218
	v_mul_f32_e64 v251, -v219, v219
	v_add_f32_e32 v246, v214, v218
	v_add_f32_e32 v252, v215, v219
	v_fma_f32 v245, -v214, v214, v245
	v_fma_f32 v251, -v215, v215, v251
	v_fma_f32 v247, v10, v246, v11
	v_fma_f32 v253, v10, v252, v11
	v_fma_f32 v246, v13, v226, v14
	v_fma_f32 v252, v13, v227, v14
	v_fma_f32 v248, v12, v222, v245
	v_fma_f32 v254, v12, v223, v251
	v_fma_f32 v249, 2.0, v244, v247
	v_fma_f32 v255, 2.0, v250, v253
	v_sub_f32_e32 v247, v247, v245
	v_sub_f32_e32 v253, v253, v251
	v_fma_f32 v246, -2.0, v244, v246
	v_fma_f32 v252, -2.0, v250, v252
	v_mul_f32_e32 v247, v247, v248
	v_mul_f32_e32 v253, v253, v254
	v_rcp_f32_e32 v247, v247
	v_rcp_f32_e32 v253, v253
	v_mul_f32_e32 v249, v249, v246
	v_mul_f32_e32 v255, v255, v252
	v_fma_f32 v22, v249, v247, v22
	v_fma_f32 v22, v255, v253, v22
	s_waitcnt lgkmcnt(0)
	v_mfma_f32_16x16x32_f16 v[212:215], v[28:31], v[228:231], 0
	v_mfma_f32_16x16x32_f16 v[216:219], v[28:31], v[232:235], 0
	v_mfma_f32_16x16x32_f16 v[220:223], v[28:31], v[236:239], v[0:3]
	v_mfma_f32_16x16x32_f16 v[224:227], v[28:31], v[240:243], 0
	v_mfma_f32_16x16x32_f16 v[212:215], v[32:35], v[164:167], v[212:215]
	v_mfma_f32_16x16x32_f16 v[216:219], v[32:35], v[172:175], v[216:219]
	v_mfma_f32_16x16x32_f16 v[220:223], v[32:35], v[180:183], v[220:223]
	v_mfma_f32_16x16x32_f16 v[224:227], v[32:35], v[188:191], v[224:227]
	v_mul_f32_e32 v244, v196, v200
	v_mul_f32_e32 v250, v197, v201
	v_mul_f32_e64 v245, -v200, v200
	v_mul_f32_e64 v251, -v201, v201
	v_add_f32_e32 v246, v196, v200
	v_add_f32_e32 v252, v197, v201
	v_fma_f32 v245, -v196, v196, v245
	v_fma_f32 v251, -v197, v197, v251
	v_fma_f32 v247, v10, v246, v11
	v_fma_f32 v253, v10, v252, v11
	v_fma_f32 v246, v13, v208, v14
	v_fma_f32 v252, v13, v209, v14
	v_fma_f32 v248, v12, v204, v245
	v_fma_f32 v254, v12, v205, v251
	v_fma_f32 v249, 2.0, v244, v247
	v_fma_f32 v255, 2.0, v250, v253
	v_sub_f32_e32 v247, v247, v245
	v_sub_f32_e32 v253, v253, v251
	v_fma_f32 v246, -2.0, v244, v246
	v_fma_f32 v252, -2.0, v250, v252
	v_mul_f32_e32 v247, v247, v248
	v_mul_f32_e32 v253, v253, v254
	v_rcp_f32_e32 v247, v247
	v_rcp_f32_e32 v253, v253
	v_mul_f32_e32 v249, v249, v246
	v_mul_f32_e32 v255, v255, v252
	v_fma_f32 v21, v249, v247, v21
	v_fma_f32 v21, v255, v253, v21
	v_mul_f32_e32 v244, v198, v202
	v_mul_f32_e32 v250, v199, v203
	v_mul_f32_e64 v245, -v202, v202
	v_mul_f32_e64 v251, -v203, v203
	v_add_f32_e32 v246, v198, v202
	v_add_f32_e32 v252, v199, v203
	v_fma_f32 v245, -v198, v198, v245
	v_fma_f32 v251, -v199, v199, v251
	v_fma_f32 v247, v10, v246, v11
	v_fma_f32 v253, v10, v252, v11
	v_fma_f32 v246, v13, v210, v14
	v_fma_f32 v252, v13, v211, v14
	v_fma_f32 v248, v12, v206, v245
	v_fma_f32 v254, v12, v207, v251
	v_fma_f32 v249, 2.0, v244, v247
	v_fma_f32 v255, 2.0, v250, v253
	v_sub_f32_e32 v247, v247, v245
	v_sub_f32_e32 v253, v253, v251
	v_fma_f32 v246, -2.0, v244, v246
	v_fma_f32 v252, -2.0, v250, v252
	v_mul_f32_e32 v247, v247, v248
	v_mul_f32_e32 v253, v253, v254
	v_rcp_f32_e32 v247, v247
	v_rcp_f32_e32 v253, v253
	v_mul_f32_e32 v249, v249, v246
	v_mul_f32_e32 v255, v255, v252
	v_fma_f32 v22, v249, v247, v22
	v_fma_f32 v22, v255, v253, v22
	v_mul_f32_e32 v244, v212, v216
	v_mul_f32_e32 v250, v213, v217
	v_mul_f32_e64 v245, -v216, v216
	v_mul_f32_e64 v251, -v217, v217
	v_add_f32_e32 v246, v212, v216
	v_add_f32_e32 v252, v213, v217
	v_fma_f32 v245, -v212, v212, v245
	v_fma_f32 v251, -v213, v213, v251
	v_fma_f32 v247, v10, v246, v11
	v_fma_f32 v253, v10, v252, v11
	v_fma_f32 v246, v13, v224, v14
	v_fma_f32 v252, v13, v225, v14
	v_fma_f32 v248, v12, v220, v245
	v_fma_f32 v254, v12, v221, v251
	v_fma_f32 v249, 2.0, v244, v247
	v_fma_f32 v255, 2.0, v250, v253
	v_sub_f32_e32 v247, v247, v245
	v_sub_f32_e32 v253, v253, v251
	v_fma_f32 v246, -2.0, v244, v246
	v_fma_f32 v252, -2.0, v250, v252
	v_mul_f32_e32 v247, v247, v248
	v_mul_f32_e32 v253, v253, v254
	v_rcp_f32_e32 v247, v247
	v_rcp_f32_e32 v253, v253
	v_mul_f32_e32 v249, v249, v246
	v_mul_f32_e32 v255, v255, v252
	v_mul_f32_e32 v249, v249, v247
	v_mul_f32_e32 v255, v255, v253
	v_fma_f32 v21, v249, v15, v21
	v_fma_f32 v21, v255, v16, v21
	v_mul_f32_e32 v244, v214, v218
	v_mul_f32_e32 v250, v215, v219
	v_mul_f32_e64 v245, -v218, v218
	v_mul_f32_e64 v251, -v219, v219
	v_add_f32_e32 v246, v214, v218
	v_add_f32_e32 v252, v215, v219
	v_fma_f32 v245, -v214, v214, v245
	v_fma_f32 v251, -v215, v215, v251
	v_fma_f32 v247, v10, v246, v11
	v_fma_f32 v253, v10, v252, v11
	v_fma_f32 v246, v13, v226, v14
	v_fma_f32 v252, v13, v227, v14
	v_fma_f32 v248, v12, v222, v245
	v_fma_f32 v254, v12, v223, v251
	v_fma_f32 v249, 2.0, v244, v247
	v_fma_f32 v255, 2.0, v250, v253
	v_sub_f32_e32 v247, v247, v245
	v_sub_f32_e32 v253, v253, v251
	v_fma_f32 v246, -2.0, v244, v246
	v_fma_f32 v252, -2.0, v250, v252
	v_mul_f32_e32 v247, v247, v248
	v_mul_f32_e32 v253, v253, v254
	v_rcp_f32_e32 v247, v247
	v_rcp_f32_e32 v253, v253
	v_mul_f32_e32 v249, v249, v246
	v_mul_f32_e32 v255, v255, v252
	v_mul_f32_e32 v249, v249, v247
	v_mul_f32_e32 v255, v255, v253
	v_fma_f32 v22, v249, v17, v22
	v_fma_f32 v22, v255, v18, v22
	v_add_f32_e32 v19, v19, v20
	v_add_f32_e32 v21, v21, v22
	v_and_b32_e32 v23, 15, v8
	s_cmp_eq_u32 s15, 7
	s_cselect_b32 s23, 6, 16
	v_cmp_gt_u32_e32 vcc, s23, v23
	s_nop 1
	v_cndmask_b32_e32 v21, 0, v21, vcc
	v_add_f32_e32 v19, v19, v21
	s_nop 1
	v_add_f32_dpp v19, v19, v19 quad_perm:[1,0,3,2] row_mask:0xf bank_mask:0xf
	s_nop 1
	v_add_f32_dpp v19, v19, v19 quad_perm:[2,3,0,1] row_mask:0xf bank_mask:0xf
	s_nop 1
	v_add_f32_dpp v19, v19, v19 row_half_mirror row_mask:0xf bank_mask:0xf
	s_nop 1
	v_add_f32_dpp v19, v19, v19 row_mirror row_mask:0xf bank_mask:0xf
	s_nop 0
	v_readlane_b32 s40, v19, 0
	v_readlane_b32 s41, v19, 16
	v_readlane_b32 s42, v19, 32
	v_readlane_b32 s43, v19, 48
	s_lshl_b32 s24, s2, 3
	s_add_u32 s24, s24, s52
	s_lshl_b32 s24, s24, 2
	v_mov_b32_e32 v19, s40
	v_add_f32_e32 v19, s41, v19
	v_add_f32_e32 v19, s42, v19
	v_add_f32_e32 v19, s43, v19
	v_mov_b32_e32 v9, s24
	v_cmp_eq_u32_e32 vcc, 0, v8
	s_nop 1
	s_and_saveexec_b64 s[30:31], vcc
	global_store_dword v9, v19, s[10:11] sc0 sc1
	s_endpgm
